# router logits: all 32 row pieces of a token group in flight before the first MFMA (was 2 at a time), LDS fragment reads one step ahead
# speedup vs baseline: 1.0078x; 1.0015x over previous
; __device__ __forceinline__ void router_phase(Frame& F, const bf16_t* H, int layer, int row0) {
;     ...
;     for (int g = F.wave * F.G + F.bid; g < ng; g += F.NGW) {
;         const int tok = row0 + g * 16 + fr;
;         const char* hp = (const char*)(H + (size_t)tok * DM) + fq * 16;
;         f32x4 acc0 = (f32x4){0.f, 0.f, 0.f, 0.f}, acc1 = (f32x4){0.f, 0.f, 0.f, 0.f};
; #pragma clang loop unroll(disable)
;         for (int half = 0; half < 2; ++half) {
;             u32x4 a[16];
; #pragma unroll
;             for (int s_ = 0; s_ < 16; ++s_) a[s_] = *(const u32x4*)(hp + half * 1024 + s_ * 64);
; #pragma unroll
;             for (int s_ = 0; s_ < 16; ++s_) {
;                 const bf16x8 w0 = *(const bf16x8*)(wb + half * 1024 + s_ * 64), w1 = *(const bf16x8*)(wb + 16 * PITCH + half * 1024 + s_ * 64);
;                 const bf16x8 hf = __builtin_bit_cast(bf16x8, a[s_]);
;                 acc0 = __builtin_amdgcn_mfma_f32_16x16x32_bf16(w0, hf, acc0, 0, 0, 0);
;                 acc1 = __builtin_amdgcn_mfma_f32_16x16x32_bf16(w1, hf, acc1, 0, 0, 0); } }
.LBB0_835:
	s_mov_b64 s[0:1], 0x400
	v_lshl_add_u64 v[40:41], v[16:17], 0, s[0:1]
	global_load_dwordx4 v[44:47], v[16:17], off
	global_load_dwordx4 v[48:51], v[16:17], off offset:64
	global_load_dwordx4 v[52:55], v[16:17], off offset:128
	global_load_dwordx4 v[56:59], v[16:17], off offset:192
	global_load_dwordx4 v[60:63], v[16:17], off offset:256
	global_load_dwordx4 v[64:67], v[16:17], off offset:320
	global_load_dwordx4 v[68:71], v[16:17], off offset:384
	global_load_dwordx4 v[72:75], v[16:17], off offset:448
	global_load_dwordx4 v[76:79], v[16:17], off offset:512
	global_load_dwordx4 v[80:83], v[16:17], off offset:576
	global_load_dwordx4 v[84:87], v[16:17], off offset:640
	global_load_dwordx4 v[88:91], v[16:17], off offset:704
	global_load_dwordx4 v[92:95], v[16:17], off offset:768
	global_load_dwordx4 v[96:99], v[16:17], off offset:832
	global_load_dwordx4 v[100:103], v[16:17], off offset:896
	global_load_dwordx4 v[104:107], v[16:17], off offset:960
	global_load_dwordx4 v[108:111], v[40:41], off
	global_load_dwordx4 v[112:115], v[40:41], off offset:64
	global_load_dwordx4 v[116:119], v[40:41], off offset:128
	global_load_dwordx4 v[120:123], v[40:41], off offset:192
	global_load_dwordx4 v[124:127], v[40:41], off offset:256
	global_load_dwordx4 v[128:131], v[40:41], off offset:320
	global_load_dwordx4 v[132:135], v[40:41], off offset:384
	global_load_dwordx4 v[136:139], v[40:41], off offset:448
	global_load_dwordx4 v[140:143], v[40:41], off offset:512
	global_load_dwordx4 v[148:151], v[40:41], off offset:576
	global_load_dwordx4 v[152:155], v[40:41], off offset:640
	global_load_dwordx4 v[156:159], v[40:41], off offset:704
	global_load_dwordx4 v[160:163], v[40:41], off offset:768
	global_load_dwordx4 v[164:167], v[40:41], off offset:832
	global_load_dwordx4 v[168:171], v[40:41], off offset:896
	global_load_dwordx4 v[172:175], v[40:41], off offset:960
	ds_read_b128 v[20:23], v18
	ds_read_b128 v[24:27], v18 offset:33024
	ds_read_b128 v[28:31], v18 offset:64
	ds_read_b128 v[32:35], v18 offset:33088
	s_waitcnt vmcnt(31) lgkmcnt(2)
	v_mfma_f32_16x16x32_bf16 v[2:5], v[20:23], v[44:47], v[2:5]
	v_mfma_f32_16x16x32_bf16 v[6:9], v[24:27], v[44:47], v[6:9]
	ds_read_b128 v[20:23], v18 offset:128
	ds_read_b128 v[24:27], v18 offset:33152
	s_waitcnt vmcnt(30) lgkmcnt(2)
	v_mfma_f32_16x16x32_bf16 v[2:5], v[28:31], v[48:51], v[2:5]
	v_mfma_f32_16x16x32_bf16 v[6:9], v[32:35], v[48:51], v[6:9]
	ds_read_b128 v[28:31], v18 offset:192
	ds_read_b128 v[32:35], v18 offset:33216
	s_waitcnt vmcnt(29) lgkmcnt(2)
	v_mfma_f32_16x16x32_bf16 v[2:5], v[20:23], v[52:55], v[2:5]
	v_mfma_f32_16x16x32_bf16 v[6:9], v[24:27], v[52:55], v[6:9]
	ds_read_b128 v[20:23], v18 offset:256
	ds_read_b128 v[24:27], v18 offset:33280
	s_waitcnt vmcnt(28) lgkmcnt(2)
	v_mfma_f32_16x16x32_bf16 v[2:5], v[28:31], v[56:59], v[2:5]
	v_mfma_f32_16x16x32_bf16 v[6:9], v[32:35], v[56:59], v[6:9]
	ds_read_b128 v[28:31], v18 offset:320
	ds_read_b128 v[32:35], v18 offset:33344
	s_waitcnt vmcnt(27) lgkmcnt(2)
	v_mfma_f32_16x16x32_bf16 v[2:5], v[20:23], v[60:63], v[2:5]
	v_mfma_f32_16x16x32_bf16 v[6:9], v[24:27], v[60:63], v[6:9]
	ds_read_b128 v[20:23], v18 offset:384
	ds_read_b128 v[24:27], v18 offset:33408
	s_waitcnt vmcnt(26) lgkmcnt(2)
	v_mfma_f32_16x16x32_bf16 v[2:5], v[28:31], v[64:67], v[2:5]
	v_mfma_f32_16x16x32_bf16 v[6:9], v[32:35], v[64:67], v[6:9]
	ds_read_b128 v[28:31], v18 offset:448
	ds_read_b128 v[32:35], v18 offset:33472
	s_waitcnt vmcnt(25) lgkmcnt(2)
	v_mfma_f32_16x16x32_bf16 v[2:5], v[20:23], v[68:71], v[2:5]
	v_mfma_f32_16x16x32_bf16 v[6:9], v[24:27], v[68:71], v[6:9]
	ds_read_b128 v[20:23], v18 offset:512
	ds_read_b128 v[24:27], v18 offset:33536
	s_waitcnt vmcnt(24) lgkmcnt(2)
	v_mfma_f32_16x16x32_bf16 v[2:5], v[28:31], v[72:75], v[2:5]
	v_mfma_f32_16x16x32_bf16 v[6:9], v[32:35], v[72:75], v[6:9]
	ds_read_b128 v[28:31], v18 offset:576
	ds_read_b128 v[32:35], v18 offset:33600
	s_waitcnt vmcnt(23) lgkmcnt(2)
	v_mfma_f32_16x16x32_bf16 v[2:5], v[20:23], v[76:79], v[2:5]
	v_mfma_f32_16x16x32_bf16 v[6:9], v[24:27], v[76:79], v[6:9]
	ds_read_b128 v[20:23], v18 offset:640
	ds_read_b128 v[24:27], v18 offset:33664
	s_waitcnt vmcnt(22) lgkmcnt(2)
	v_mfma_f32_16x16x32_bf16 v[2:5], v[28:31], v[80:83], v[2:5]
	v_mfma_f32_16x16x32_bf16 v[6:9], v[32:35], v[80:83], v[6:9]
	ds_read_b128 v[28:31], v18 offset:704
	ds_read_b128 v[32:35], v18 offset:33728
	s_waitcnt vmcnt(21) lgkmcnt(2)
	v_mfma_f32_16x16x32_bf16 v[2:5], v[20:23], v[84:87], v[2:5]
	v_mfma_f32_16x16x32_bf16 v[6:9], v[24:27], v[84:87], v[6:9]
	ds_read_b128 v[20:23], v18 offset:768
	ds_read_b128 v[24:27], v18 offset:33792
	s_waitcnt vmcnt(20) lgkmcnt(2)
	v_mfma_f32_16x16x32_bf16 v[2:5], v[28:31], v[88:91], v[2:5]
	v_mfma_f32_16x16x32_bf16 v[6:9], v[32:35], v[88:91], v[6:9]
	ds_read_b128 v[28:31], v18 offset:832
	ds_read_b128 v[32:35], v18 offset:33856
	s_waitcnt vmcnt(19) lgkmcnt(2)
; __device__ __forceinline__ void router_phase(Frame& F, const bf16_t* H, int layer, int row0) {
;     ...
;             for (int s_ = 0; s_ < 16; ++s_) a[s_] = *(const u32x4*)(hp + half * 1024 + s_ * 64);
; #pragma unroll
;             for (int s_ = 0; s_ < 16; ++s_) {
;                 const bf16x8 w0 = *(const bf16x8*)(wb + half * 1024 + s_ * 64), w1 = *(const bf16x8*)(wb + 16 * PITCH + half * 1024 + s_ * 64);
;                 const bf16x8 hf = __builtin_bit_cast(bf16x8, a[s_]);
;                 acc0 = __builtin_amdgcn_mfma_f32_16x16x32_bf16(w0, hf, acc0, 0, 0, 0);
;                 acc1 = __builtin_amdgcn_mfma_f32_16x16x32_bf16(w1, hf, acc1, 0, 0, 0); } }
;         *(f32x4*)(L + (size_t)tok * NEXP + 4 * fq) = acc0; *(f32x4*)(L + (size_t)tok * NEXP + 16 + 4 * fq) = acc1;
;     }
	v_mfma_f32_16x16x32_bf16 v[2:5], v[20:23], v[92:95], v[2:5]
	v_mfma_f32_16x16x32_bf16 v[6:9], v[24:27], v[92:95], v[6:9]
	ds_read_b128 v[20:23], v18 offset:896
	ds_read_b128 v[24:27], v18 offset:33920
	s_waitcnt vmcnt(18) lgkmcnt(2)
	v_mfma_f32_16x16x32_bf16 v[2:5], v[28:31], v[96:99], v[2:5]
	v_mfma_f32_16x16x32_bf16 v[6:9], v[32:35], v[96:99], v[6:9]
	ds_read_b128 v[28:31], v18 offset:960
	ds_read_b128 v[32:35], v18 offset:33984
	s_waitcnt vmcnt(17) lgkmcnt(2)
	v_mfma_f32_16x16x32_bf16 v[2:5], v[20:23], v[100:103], v[2:5]
	v_mfma_f32_16x16x32_bf16 v[6:9], v[24:27], v[100:103], v[6:9]
	ds_read_b128 v[20:23], v18 offset:1024
	ds_read_b128 v[24:27], v18 offset:34048
	s_waitcnt vmcnt(16) lgkmcnt(2)
	v_mfma_f32_16x16x32_bf16 v[2:5], v[28:31], v[104:107], v[2:5]
	v_mfma_f32_16x16x32_bf16 v[6:9], v[32:35], v[104:107], v[6:9]
	ds_read_b128 v[28:31], v18 offset:1088
	ds_read_b128 v[32:35], v18 offset:34112
	s_waitcnt vmcnt(15) lgkmcnt(2)
	v_mfma_f32_16x16x32_bf16 v[2:5], v[20:23], v[108:111], v[2:5]
	v_mfma_f32_16x16x32_bf16 v[6:9], v[24:27], v[108:111], v[6:9]
	ds_read_b128 v[20:23], v18 offset:1152
	ds_read_b128 v[24:27], v18 offset:34176
	s_waitcnt vmcnt(14) lgkmcnt(2)
	v_mfma_f32_16x16x32_bf16 v[2:5], v[28:31], v[112:115], v[2:5]
	v_mfma_f32_16x16x32_bf16 v[6:9], v[32:35], v[112:115], v[6:9]
	ds_read_b128 v[28:31], v18 offset:1216
	ds_read_b128 v[32:35], v18 offset:34240
	s_waitcnt vmcnt(13) lgkmcnt(2)
	v_mfma_f32_16x16x32_bf16 v[2:5], v[20:23], v[116:119], v[2:5]
	v_mfma_f32_16x16x32_bf16 v[6:9], v[24:27], v[116:119], v[6:9]
	ds_read_b128 v[20:23], v18 offset:1280
	ds_read_b128 v[24:27], v18 offset:34304
	s_waitcnt vmcnt(12) lgkmcnt(2)
	v_mfma_f32_16x16x32_bf16 v[2:5], v[28:31], v[120:123], v[2:5]
	v_mfma_f32_16x16x32_bf16 v[6:9], v[32:35], v[120:123], v[6:9]
	ds_read_b128 v[28:31], v18 offset:1344
	ds_read_b128 v[32:35], v18 offset:34368
	s_waitcnt vmcnt(11) lgkmcnt(2)
	v_mfma_f32_16x16x32_bf16 v[2:5], v[20:23], v[124:127], v[2:5]
	v_mfma_f32_16x16x32_bf16 v[6:9], v[24:27], v[124:127], v[6:9]
	ds_read_b128 v[20:23], v18 offset:1408
	ds_read_b128 v[24:27], v18 offset:34432
	s_waitcnt vmcnt(10) lgkmcnt(2)
	v_mfma_f32_16x16x32_bf16 v[2:5], v[28:31], v[128:131], v[2:5]
	v_mfma_f32_16x16x32_bf16 v[6:9], v[32:35], v[128:131], v[6:9]
	ds_read_b128 v[28:31], v18 offset:1472
	ds_read_b128 v[32:35], v18 offset:34496
	s_waitcnt vmcnt(9) lgkmcnt(2)
	v_mfma_f32_16x16x32_bf16 v[2:5], v[20:23], v[132:135], v[2:5]
	v_mfma_f32_16x16x32_bf16 v[6:9], v[24:27], v[132:135], v[6:9]
	ds_read_b128 v[20:23], v18 offset:1536
	ds_read_b128 v[24:27], v18 offset:34560
	s_waitcnt vmcnt(8) lgkmcnt(2)
	v_mfma_f32_16x16x32_bf16 v[2:5], v[28:31], v[136:139], v[2:5]
	v_mfma_f32_16x16x32_bf16 v[6:9], v[32:35], v[136:139], v[6:9]
	ds_read_b128 v[28:31], v18 offset:1600
	ds_read_b128 v[32:35], v18 offset:34624
	s_waitcnt vmcnt(7) lgkmcnt(2)
	v_mfma_f32_16x16x32_bf16 v[2:5], v[20:23], v[140:143], v[2:5]
	v_mfma_f32_16x16x32_bf16 v[6:9], v[24:27], v[140:143], v[6:9]
	ds_read_b128 v[20:23], v18 offset:1664
	ds_read_b128 v[24:27], v18 offset:34688
	s_waitcnt vmcnt(6) lgkmcnt(2)
	v_mfma_f32_16x16x32_bf16 v[2:5], v[28:31], v[148:151], v[2:5]
	v_mfma_f32_16x16x32_bf16 v[6:9], v[32:35], v[148:151], v[6:9]
	ds_read_b128 v[28:31], v18 offset:1728
	ds_read_b128 v[32:35], v18 offset:34752
	s_waitcnt vmcnt(5) lgkmcnt(2)
	v_mfma_f32_16x16x32_bf16 v[2:5], v[20:23], v[152:155], v[2:5]
	v_mfma_f32_16x16x32_bf16 v[6:9], v[24:27], v[152:155], v[6:9]
	ds_read_b128 v[20:23], v18 offset:1792
	ds_read_b128 v[24:27], v18 offset:34816
	s_waitcnt vmcnt(4) lgkmcnt(2)
	v_mfma_f32_16x16x32_bf16 v[2:5], v[28:31], v[156:159], v[2:5]
	v_mfma_f32_16x16x32_bf16 v[6:9], v[32:35], v[156:159], v[6:9]
	ds_read_b128 v[28:31], v18 offset:1856
	ds_read_b128 v[32:35], v18 offset:34880
	s_waitcnt vmcnt(3) lgkmcnt(2)
	v_mfma_f32_16x16x32_bf16 v[2:5], v[20:23], v[160:163], v[2:5]
	v_mfma_f32_16x16x32_bf16 v[6:9], v[24:27], v[160:163], v[6:9]
	ds_read_b128 v[20:23], v18 offset:1920
	ds_read_b128 v[24:27], v18 offset:34944
	s_waitcnt vmcnt(2) lgkmcnt(2)
	v_mfma_f32_16x16x32_bf16 v[2:5], v[28:31], v[164:167], v[2:5]
	v_mfma_f32_16x16x32_bf16 v[6:9], v[32:35], v[164:167], v[6:9]
	ds_read_b128 v[28:31], v18 offset:1984
	ds_read_b128 v[32:35], v18 offset:35008
	s_waitcnt vmcnt(1) lgkmcnt(2)
	v_mfma_f32_16x16x32_bf16 v[2:5], v[20:23], v[168:171], v[2:5]
	v_mfma_f32_16x16x32_bf16 v[6:9], v[24:27], v[168:171], v[6:9]
	s_waitcnt vmcnt(0) lgkmcnt(0)
	v_mfma_f32_16x16x32_bf16 v[2:5], v[28:31], v[172:175], v[2:5]
	v_mfma_f32_16x16x32_bf16 v[6:9], v[32:35], v[172:175], v[6:9]
	v_lshlrev_b64 v[14:15], 7, v[14:15]
	s_add_i32 s5, s5, s7
	v_lshl_add_u64 v[14:15], v[12:13], 0, v[14:15]
	s_cmp_ge_i32 s5, s4
	s_nop 0
	global_store_dwordx4 v[14:15], v[2:5], off
	s_nop 0
	global_store_dwordx4 v[14:15], v[6:9], off offset:64
	s_cbranch_scc0 .LBB0_834
